# P9 slot lists: the four expert-id loads and the four slot-weight loads issued together with counted waits (was load -> vmcnt(0) -> use, eight serial round trips)
# baseline (speedup 1.0000x reference)
; __global__ void __launch_bounds__(NW * 64, 2) mk_fwd(Args args) {
;     ...
;         for (int c0 = bx * 2048; c0 < NSLOT; c0 += G * 2048) {
;             __syncthreads();
;             if (tid < NE) hist[tid] = 0u;
;             __syncthreads();
;             int e[4]; unsigned loc[4];
; #pragma unroll
;             for (int i = 0; i < 4; ++i) { const int idx = c0 + i * 512 + tid; e[i] = topk_e[idx]; loc[i] = __hip_atomic_fetch_add(&hist[e[i]], 1u, __ATOMIC_RELAXED, __HIP_MEMORY_SCOPE_WORKGROUP); }
;             __syncthreads();
;             if (tid < NE && hist[tid]) base[tid] = atomicAdd(&ctl[CW_CURSOR + tid], hist[tid]);
;             __syncthreads();
; #pragma unroll
;             for (int i = 0; i < 4; ++i) { const int idx = c0 + i * 512 + tid; const unsigned pos = tab[T_OFF + e[i]] + base[e[i]] + loc[i]; slot_ent[pos] = idx; slot_w[pos] = topk_w[idx]; }
;         }
.LBB0_508:
	s_or_b64 exec, exec, s[2:3]
	v_lshl_add_u64 v[24:25], v[4:5], 2, s[14:15]
	s_waitcnt lgkmcnt(0)
	s_barrier
	global_load_dword v30, v[24:25], off
	v_lshl_add_u64 v[24:25], v[6:7], 2, s[14:15]
	global_load_dword v31, v[24:25], off
	v_lshl_add_u64 v[24:25], v[8:9], 2, s[14:15]
	global_load_dword v32, v[24:25], off
	v_lshl_add_u64 v[24:25], v[10:11], 2, s[14:15]
	global_load_dword v33, v[24:25], off
	v_lshlrev_b32_e32 v22, 2, v22
	v_add_u32_e32 v23, s18, v22
	v_add_u32_e32 v22, s17, v22
	ds_read_b32 v24, v23
	ds_read_b32 v25, v22
	v_lshl_add_u64 v[22:23], v[6:7], 2, s[14:15]
	s_add_i32 s1, s1, s0
	s_cmp_lt_i32 s1, 0x80000
	s_waitcnt lgkmcnt(0)
	v_add3_u32 v2, v25, v24, v2
	v_lshlrev_b64 v[24:25], 2, v[2:3]
	v_lshl_add_u64 v[26:27], s[10:11], 0, v[24:25]
	v_lshlrev_b32_e32 v2, 2, v21
	v_add_u32_e32 v7, s18, v2
	v_add_u32_e32 v2, s17, v2
	s_waitcnt vmcnt(3)
	global_store_dword v[26:27], v30, off
	ds_read_b32 v7, v7
	ds_read_b32 v2, v2
	v_lshl_add_u64 v[22:23], v[8:9], 2, s[14:15]
	s_waitcnt lgkmcnt(0)
	v_add3_u32 v2, v2, v7, v20
	v_lshlrev_b64 v[20:21], 2, v[2:3]
	v_lshl_add_u64 v[26:27], s[10:11], 0, v[20:21]
	v_lshlrev_b32_e32 v2, 2, v18
	v_add_u32_e32 v7, s18, v2
	v_add_u32_e32 v2, s17, v2
	s_waitcnt vmcnt(3)
	global_store_dword v[26:27], v31, off
	ds_read_b32 v7, v7
	ds_read_b32 v2, v2
	s_waitcnt lgkmcnt(0)
	v_add3_u32 v2, v2, v7, v19
	v_lshlrev_b64 v[18:19], 2, v[2:3]
	v_lshl_add_u64 v[22:23], s[10:11], 0, v[18:19]
	v_lshlrev_b32_e32 v2, 2, v17
	s_waitcnt vmcnt(3)
	global_store_dword v[22:23], v32, off
	v_lshl_add_u64 v[22:23], v[10:11], 2, s[14:15]
	v_lshl_add_u64 v[22:23], s[4:5], 0, v[24:25]
	global_store_dword v[22:23], v4, off
	v_add_u32_e32 v4, s18, v2
	v_add_u32_e32 v2, s17, v2
	ds_read_b32 v7, v4
	ds_read_b32 v2, v2
	v_lshl_add_u64 v[4:5], s[4:5], 0, v[20:21]
	global_store_dword v[4:5], v6, off
	v_lshl_add_u64 v[4:5], s[4:5], 0, v[18:19]
	global_store_dword v[4:5], v8, off
	s_waitcnt lgkmcnt(0)
	v_add3_u32 v2, v2, v7, v16
	v_lshlrev_b64 v[4:5], 2, v[2:3]
	v_lshl_add_u64 v[6:7], s[4:5], 0, v[4:5]
	v_lshl_add_u64 v[4:5], s[10:11], 0, v[4:5]
	global_store_dword v[6:7], v10, off
	s_waitcnt vmcnt(7)
	global_store_dword v[4:5], v33, off
	s_cbranch_scc0 .LBB0_514
.LBB0_509:
	s_barrier
	s_and_saveexec_b64 s[2:3], vcc
	ds_write_b32 v15, v3
	s_or_b64 exec, exec, s[2:3]
	v_add_u32_e32 v4, s1, v12
	v_ashrrev_i32_e32 v5, 31, v4
	v_lshl_add_u64 v[6:7], v[4:5], 2, s[12:13]
	s_waitcnt lgkmcnt(0)
	s_barrier
	global_load_dword v22, v[6:7], off
	v_add_u32_e32 v6, 0x200, v4
	v_ashrrev_i32_e32 v7, 31, v6
	v_lshl_add_u64 v[28:29], v[6:7], 2, s[12:13]
	global_load_dword v21, v[28:29], off
	v_add_u32_e32 v8, 0x400, v4
	v_ashrrev_i32_e32 v9, 31, v8
	v_lshl_add_u64 v[28:29], v[8:9], 2, s[12:13]
	global_load_dword v18, v[28:29], off
	v_add_u32_e32 v10, 0x600, v4
	v_ashrrev_i32_e32 v11, 31, v10
	v_lshl_add_u64 v[28:29], v[10:11], 2, s[12:13]
	global_load_dword v17, v[28:29], off
	s_waitcnt vmcnt(3)
	v_lshl_add_u32 v2, v22, 2, s16
	ds_add_rtn_u32 v2, v2, v13
	s_waitcnt vmcnt(2)
	v_lshl_add_u32 v16, v21, 2, s16
	ds_add_rtn_u32 v20, v16, v13
	s_waitcnt vmcnt(1)
	v_lshl_add_u32 v16, v18, 2, s16
	ds_add_rtn_u32 v19, v16, v13
	s_waitcnt vmcnt(0)
	v_lshl_add_u32 v16, v17, 2, s16
	ds_add_rtn_u32 v16, v16, v13
	s_waitcnt lgkmcnt(0)
	s_barrier
	s_and_saveexec_b64 s[2:3], vcc
	s_cbranch_execz .LBB0_508
	ds_read_b32 v23, v15
	s_waitcnt lgkmcnt(0)
	v_cmp_ne_u32_e64 s[8:9], 0, v23
	s_and_b64 exec, exec, s[8:9]
	s_cbranch_execz .LBB0_508
	global_atomic_add v23, v[0:1], v23, off sc0
	s_waitcnt vmcnt(0)
	ds_write_b32 v14, v23
	s_branch .LBB0_508
